# v18
# speedup vs baseline: 1.0219x; 1.0009x over previous
.LBB1_3:
	s_waitcnt lgkmcnt(0)
	v_lshrrev_b32_e32 v3, 4, v0
	v_and_b32_e32 v4, 15, v0
	v_bfe_u32 v5, v0, 4, 2
	v_and_b32_e32 v7, 7, v0
	s_lshl_b32 s0, s30, 5
	s_sext_i32_i16 s76, s28
	v_lshl_or_b32 v207, s31, 6, v4
	v_bitop3_b32 v3, v3, v7, 3 bitop3:0x6c
	v_bitop3_b32 v7, v5, v7, 4 bitop3:0x36
	s_and_b32 s28, s0, 0x60
	v_lshlrev_b32_e32 v6, 7, v207
	v_lshlrev_b32_e32 v3, 4, v3
	v_lshlrev_b32_e32 v7, 4, v7
	v_or_b32_e32 v4, s28, v4
	s_cmp_lg_u32 s16, 0
	v_lshlrev_b32_e32 v206, 2, v0
	v_lshlrev_b32_e32 v230, 4, v0
	v_lshlrev_b32_e32 v231, 3, v0
	v_lshlrev_b32_e32 v0, 4, v0
	v_or_b32_e32 v8, v6, v3
	v_or_b32_e32 v6, v6, v7
	v_lshlrev_b32_e32 v4, 7, v4
	s_cselect_b64 s[0:1], -1, 0
	v_add_u32_e32 v208, v2, v1
	v_add_u32_e32 v0, 0, v0
	v_or_b32_e32 v222, v4, v3
	v_or_b32_e32 v223, v4, v7
	v_add_u32_e32 v228, 0x10000, v222
	v_add_u32_e32 v229, 0x10000, v223
	s_mul_i32 s65, s2, 0x70
	v_lshl_or_b32 v224, v5, 3, s28
	v_add_u32_e32 v210, 0x80000, v208
	v_mov_b32_e32 v211, v205
	v_mov_b32_e32 v209, v205
	s_and_b64 s[0:1], exec, s[0:1]
	s_movk_i32 s16, 0xe00
	v_add_u32_e32 v225, 0x20000, v0
	s_add_i32 s66, 0, 0x10000
	s_add_i32 s67, 0, 0x10800
	s_add_i32 s68, 0, 0x14000
	s_add_i32 s69, 0, 0x14800
	s_add_i32 s70, 0, 0x18000
	s_add_i32 s71, 0, 0x18800
	s_add_i32 s72, 0, 0x1c000
	s_add_i32 s73, 0, 0x1c800
	s_movk_i32 s74, 0x7000
	v_add_u32_e32 v226, 0, v8
	v_add_u32_e32 v227, 0, v6
	s_mov_b32 s30, s29
	s_mov_b32 s34, s29
	s_mov_b32 s28, 0
	s_branch .LBB1_5

.LBB1_9:
	s_add_i32 s82, s48, 2
	s_and_b32 s28, s82, 2
	s_bitcmp1_b32 s82, 1
	s_cselect_b64 s[4:5], -1, 0
	s_cmp_eq_u32 s28, 0
	s_cbranch_scc1 .LBB1_14
	ds_read_b128 v[0:3], v225
.LBB1_14:
	ds_read_b128 v[148:151], v228
	ds_read_b128 v[152:155], v229
	ds_read_b128 v[156:159], v228 offset:2048
	ds_read_b128 v[160:163], v229 offset:2048
	s_add_i32 m0, s43, 0xc000
	ds_read_b128 v[132:135], v228 offset:16384
	ds_read_b128 v[136:139], v229 offset:16384
	ds_read_b128 v[140:143], v228 offset:18432
	ds_read_b128 v[144:147], v229 offset:18432
	ds_read_b128 v[166:169], v226
	ds_read_b128 v[170:173], v226 offset:2048
	ds_read_b128 v[174:177], v227
	ds_read_b128 v[178:181], v227 offset:2048
	ds_read_b128 v[182:185], v226 offset:4096
	ds_read_b128 v[186:189], v226 offset:6144
	ds_read_b128 v[190:193], v227 offset:4096
	ds_read_b128 v[214:217], v227 offset:6144
	global_load_lds_dwordx4 v208, s[44:45]
	s_add_i32 m0, s43, 0xe000
	s_nop 0
	global_load_lds_dwordx4 v210, s[44:45]
	s_lshr_b32 s94, s82, 2
	s_add_i32 s94, s94, s79
	s_mov_b64 vcc, s[0:1]
	s_cbranch_vccz .LBB1_26
	s_mul_hi_i32 s95, s94, 0x92492493
	s_add_i32 s95, s95, s94
	s_lshr_b32 s28, s95, 31
	s_ashr_i32 s95, s95, 12
	s_add_i32 s95, s95, s28
	s_mul_i32 s28, s95, 0x1c00
	s_sub_i32 s46, s94, s28
	s_bitcmp0_b32 s95, 0
	s_cselect_b32 s28, s16, 0x2a00
	s_ashr_i32 s49, s46, 1
	s_lshl_b32 s46, s46, 11
	s_add_i32 s28, s28, s49
	s_and_b32 s92, s46, 0x800
	s_cmp_lt_u32 s95, 2
	s_cselect_b32 s50, s9, s11
	s_cselect_b32 s51, s8, s10
	s_lshl_b64 s[46:47], s[28:29], 14
	s_add_u32 s46, s51, s46
	s_addc_u32 s47, s50, s47
	s_lshl_b32 s93, s92, 2
	s_add_u32 s88, s46, s93
	s_addc_u32 s89, s47, 0
	s_lshl_b32 s95, s95, 6
	s_lshl_b32 s28, s28, 1
	s_and_b32 s46, s49, 0x7f
	s_and_b32 s95, s95, 0xffffff80
	s_and_b32 s28, s28, 0x7fffff00
	s_or_b32 s95, s95, s46
	s_add_i32 s46, s95, s28
	s_ashr_i32 s47, s46, 31
	s_lshl_b64 s[46:47], s[46:47], 13
	s_add_u32 s46, s14, s46
	s_addc_u32 s47, s15, s47
	s_lshl_b32 s93, s92, 1
	s_add_u32 s90, s46, s93
	s_addc_u32 s91, s47, 0
	s_branch .LBB1_12
.LBB1_11:
	s_ashr_i32 s95, s94, 31
	s_lshl_b64 s[94:95], s[94:95], 11
	s_lshl_b64 s[88:89], s[94:95], 2
	s_add_u32 s88, s88, s12
	s_addc_u32 s89, s89, s13
	s_lshl_b64 s[90:91], s[94:95], 1
	s_add_u32 s90, s90, s26
	s_addc_u32 s91, s91, s27
.LBB1_12:
	s_waitcnt vmcnt(8)
	s_waitcnt lgkmcnt(0)
	s_barrier
	s_setprio 1
	s_waitcnt lgkmcnt(0)
	v_mfma_f32_16x16x32_f16 v[128:131], v[148:151], v[166:169], v[128:131]
	v_mfma_f32_16x16x32_f16 v[128:131], v[152:155], v[174:177], v[128:131]
	v_mfma_f32_16x16x32_f16 v[120:123], v[160:163], v[174:177], v[120:123]
	v_mfma_f32_16x16x32_f16 v[120:123], v[156:159], v[166:169], v[120:123]
	v_mfma_f32_16x16x32_f16 v[104:107], v[156:159], v[170:173], v[104:107]
	v_mfma_f32_16x16x32_f16 v[104:107], v[160:163], v[178:181], v[104:107]
	v_mfma_f32_16x16x32_f16 v[112:115], v[152:155], v[178:181], v[112:115]
	v_mfma_f32_16x16x32_f16 v[112:115], v[148:151], v[170:173], v[112:115]
	v_mfma_f32_16x16x32_f16 v[96:99], v[148:151], v[182:185], v[96:99]
	v_mfma_f32_16x16x32_f16 v[96:99], v[152:155], v[190:193], v[96:99]
	v_mfma_f32_16x16x32_f16 v[88:91], v[160:163], v[190:193], v[88:91]
	v_mfma_f32_16x16x32_f16 v[88:91], v[156:159], v[182:185], v[88:91]
	v_mfma_f32_16x16x32_f16 v[72:75], v[156:159], v[186:189], v[72:75]
	v_mfma_f32_16x16x32_f16 v[72:75], v[160:163], v[214:217], v[72:75]
	v_mfma_f32_16x16x32_f16 v[80:83], v[152:155], v[214:217], v[80:83]
	v_mfma_f32_16x16x32_f16 v[80:83], v[148:151], v[186:189], v[80:83]
	s_setprio 0
	s_setprio 1
	v_mfma_f32_16x16x32_f16 v[124:127], v[132:135], v[166:169], v[124:127]
	v_mfma_f32_16x16x32_f16 v[124:127], v[136:139], v[174:177], v[124:127]
	v_mfma_f32_16x16x32_f16 v[116:119], v[144:147], v[174:177], v[116:119]
	v_mfma_f32_16x16x32_f16 v[116:119], v[140:143], v[166:169], v[116:119]
	v_mfma_f32_16x16x32_f16 v[100:103], v[140:143], v[170:173], v[100:103]
	v_mfma_f32_16x16x32_f16 v[100:103], v[144:147], v[178:181], v[100:103]
	v_mfma_f32_16x16x32_f16 v[108:111], v[136:139], v[178:181], v[108:111]
	v_mfma_f32_16x16x32_f16 v[108:111], v[132:135], v[170:173], v[108:111]
	v_mfma_f32_16x16x32_f16 v[92:95], v[132:135], v[182:185], v[92:95]
	v_mfma_f32_16x16x32_f16 v[92:95], v[136:139], v[190:193], v[92:95]
	v_mfma_f32_16x16x32_f16 v[84:87], v[144:147], v[190:193], v[84:87]
	v_mfma_f32_16x16x32_f16 v[84:87], v[140:143], v[182:185], v[84:87]
	v_mfma_f32_16x16x32_f16 v[68:71], v[140:143], v[186:189], v[68:71]
	v_mfma_f32_16x16x32_f16 v[68:71], v[144:147], v[214:217], v[68:71]
	v_mfma_f32_16x16x32_f16 v[76:79], v[136:139], v[214:217], v[76:79]
	v_mfma_f32_16x16x32_f16 v[76:79], v[132:135], v[186:189], v[76:79]
	s_setprio 0
	s_barrier
	s_andn2_b64 vcc, exec, s[4:5]
	s_cbranch_vccnz .LBB1_16
	v_cvt_pkrtz_f16_f32 v166, v0, v1
	v_cvt_pkrtz_f16_f32 v167, v2, v3
	v_add_u32_e32 v166, 0x20002, v166
	v_add_u32_e32 v167, 0x20002, v167
	v_and_b32_e32 v166, 0xfffcfffc, v166
	v_and_b32_e32 v167, 0xfffcfffc, v167
	global_store_dwordx2 v231, v[166:167], s[90:91]

	.amdhsa_kernel _Z12gemm_persistILi0ELi4096ELi32ELi112EEvPKDF16_S1_PvPKfS4_S4_S4_PDF16_S5_iii
		.amdhsa_group_segment_fixed_size 0
		.amdhsa_private_segment_fixed_size 0
		.amdhsa_kernarg_size 344
		.amdhsa_user_sgpr_count 2
		.amdhsa_user_sgpr_dispatch_ptr 0
		.amdhsa_user_sgpr_queue_ptr 0
		.amdhsa_user_sgpr_kernarg_segment_ptr 1
		.amdhsa_user_sgpr_dispatch_id 0
		.amdhsa_user_sgpr_kernarg_preload_length 0
		.amdhsa_user_sgpr_kernarg_preload_offset 0
		.amdhsa_user_sgpr_private_segment_size 0
		.amdhsa_uses_dynamic_stack 0
		.amdhsa_enable_private_segment 0
		.amdhsa_system_sgpr_workgroup_id_x 1
		.amdhsa_system_sgpr_workgroup_id_y 0
		.amdhsa_system_sgpr_workgroup_id_z 0
		.amdhsa_system_sgpr_workgroup_info 0
		.amdhsa_system_vgpr_workitem_id 0
		.amdhsa_next_free_vgpr 232
		.amdhsa_next_free_sgpr 96
		.amdhsa_accum_offset 232
		.amdhsa_reserve_vcc 1
		.amdhsa_float_round_mode_32 0
		.amdhsa_float_round_mode_16_64 0
		.amdhsa_float_denorm_mode_32 3
		.amdhsa_float_denorm_mode_16_64 3
		.amdhsa_dx10_clamp 1
		.amdhsa_ieee_mode 1
		.amdhsa_fp16_overflow 0
		.amdhsa_tg_split 0
		.amdhsa_exception_fp_ieee_invalid_op 0
		.amdhsa_exception_fp_denorm_src 0
		.amdhsa_exception_fp_ieee_div_zero 0
		.amdhsa_exception_fp_ieee_overflow 0
		.amdhsa_exception_fp_ieee_underflow 0
		.amdhsa_exception_fp_ieee_inexact 0
		.amdhsa_exception_int_div_zero 0
	.end_amdhsa_kernel

amdhsa.kernels:
  - .agpr_count:     4
    .args:
      - .actual_access:  read_only
        .address_space:  global
        .offset:         0
        .size:           8
        .value_kind:     global_buffer
      - .actual_access:  read_only
        .address_space:  global
        .offset:         8
        .size:           8
        .value_kind:     global_buffer
      - .actual_access:  read_only
        .address_space:  global
        .offset:         16
        .size:           8
        .value_kind:     global_buffer
      - .actual_access:  read_only
        .address_space:  global
        .offset:         24
        .size:           8
        .value_kind:     global_buffer
      - .actual_access:  write_only
        .address_space:  global
        .offset:         32
        .size:           8
        .value_kind:     global_buffer
      - .actual_access:  write_only
        .address_space:  global
        .offset:         40
        .size:           8
        .value_kind:     global_buffer
      - .actual_access:  write_only
        .address_space:  global
        .offset:         48
        .size:           8
        .value_kind:     global_buffer
    .group_segment_fixed_size: 4352
    .kernarg_segment_align: 8
    .kernarg_segment_size: 56
    .language:       OpenCL C
    .language_version:
      - 2
      - 0
    .max_flat_workgroup_size: 256
    .name:           _Z11prep_kernelPKfS0_S0_S0_PDF16_PfS1_
    .private_segment_fixed_size: 0
    .sgpr_count:     26
    .sgpr_spill_count: 0
    .symbol:         _Z11prep_kernelPKfS0_S0_S0_PDF16_PfS1_.kd
    .uniform_work_group_size: 1
    .uses_dynamic_stack: false
    .vgpr_count:     56
    .vgpr_spill_count: 0
    .wavefront_size: 64
  - .agpr_count:     0
    .args:
      - .address_space:  global
        .offset:         0
        .size:           8
        .value_kind:     global_buffer
      - .address_space:  global
        .offset:         8
        .size:           8
        .value_kind:     global_buffer
      - .actual_access:  write_only
        .address_space:  global
        .offset:         16
        .size:           8
        .value_kind:     global_buffer
      - .actual_access:  read_only
        .address_space:  global
        .offset:         24
        .size:           8
        .value_kind:     global_buffer
      - .address_space:  global
        .offset:         32
        .size:           8
        .value_kind:     global_buffer
      - .address_space:  global
        .offset:         40
        .size:           8
        .value_kind:     global_buffer
      - .address_space:  global
        .offset:         48
        .size:           8
        .value_kind:     global_buffer
      - .actual_access:  write_only
        .address_space:  global
        .offset:         56
        .size:           8
        .value_kind:     global_buffer
      - .actual_access:  write_only
        .address_space:  global
        .offset:         64
        .size:           8
        .value_kind:     global_buffer
      - .offset:         72
        .size:           4
        .value_kind:     by_value
      - .offset:         76
        .size:           4
        .value_kind:     by_value
      - .offset:         80
        .size:           4
        .value_kind:     by_value
      - .offset:         88
        .size:           4
        .value_kind:     hidden_block_count_x
      - .offset:         92
        .size:           4
        .value_kind:     hidden_block_count_y
      - .offset:         96
        .size:           4
        .value_kind:     hidden_block_count_z
      - .offset:         100
        .size:           2
        .value_kind:     hidden_group_size_x
      - .offset:         102
        .size:           2
        .value_kind:     hidden_group_size_y
      - .offset:         104
        .size:           2
        .value_kind:     hidden_group_size_z
      - .offset:         106
        .size:           2
        .value_kind:     hidden_remainder_x
      - .offset:         108
        .size:           2
        .value_kind:     hidden_remainder_y
      - .offset:         110
        .size:           2
        .value_kind:     hidden_remainder_z
      - .offset:         128
        .size:           8
        .value_kind:     hidden_global_offset_x
      - .offset:         136
        .size:           8
        .value_kind:     hidden_global_offset_y
      - .offset:         144
        .size:           8
        .value_kind:     hidden_global_offset_z
      - .offset:         152
        .size:           2
        .value_kind:     hidden_grid_dims
      - .offset:         208
        .size:           4
        .value_kind:     hidden_dynamic_lds_size
    .group_segment_fixed_size: 0
    .kernarg_segment_align: 8
    .kernarg_segment_size: 344
    .language:       OpenCL C
    .language_version:
      - 2
      - 0
    .max_flat_workgroup_size: 512
    .name:           _Z12gemm_persistILi0ELi4096ELi32ELi112EEvPKDF16_S1_PvPKfS4_S4_S4_PDF16_S5_iii
    .private_segment_fixed_size: 0
    .sgpr_count:     102
    .sgpr_spill_count: 0
    .symbol:         _Z12gemm_persistILi0ELi4096ELi32ELi112EEvPKDF16_S1_PvPKfS4_S4_S4_PDF16_S5_iii.kd
    .uniform_work_group_size: 1
    .uses_dynamic_stack: false
    .vgpr_count:     232
    .vgpr_spill_count: 0
    .wavefront_size: 64
  - .agpr_count:     0
    .args:
      - .address_space:  global
        .offset:         0
        .size:           8
        .value_kind:     global_buffer
      - .address_space:  global
        .offset:         8
        .size:           8
        .value_kind:     global_buffer
      - .actual_access:  write_only
        .address_space:  global
        .offset:         16
        .size:           8
        .value_kind:     global_buffer
      - .actual_access:  read_only
        .address_space:  global
        .offset:         24
        .size:           8
        .value_kind:     global_buffer
      - .actual_access:  read_only
        .address_space:  global
        .offset:         32
        .size:           8
        .value_kind:     global_buffer
      - .actual_access:  read_only
        .address_space:  global
        .offset:         40
        .size:           8
        .value_kind:     global_buffer
      - .actual_access:  read_only
        .address_space:  global
        .offset:         48
        .size:           8
        .value_kind:     global_buffer
      - .actual_access:  read_only
        .address_space:  global
        .offset:         56
        .size:           8
        .value_kind:     global_buffer
      - .actual_access:  read_only
        .address_space:  global
        .offset:         64
        .size:           8
        .value_kind:     global_buffer
      - .offset:         72
        .size:           4
        .value_kind:     by_value
      - .offset:         76
        .size:           4
        .value_kind:     by_value
      - .offset:         80
        .size:           4
        .value_kind:     by_value
      - .offset:         88
        .size:           4
        .value_kind:     hidden_block_count_x
      - .offset:         92
        .size:           4
        .value_kind:     hidden_block_count_y
      - .offset:         96
        .size:           4
        .value_kind:     hidden_block_count_z
      - .offset:         100
        .size:           2
        .value_kind:     hidden_group_size_x
      - .offset:         102
        .size:           2
        .value_kind:     hidden_group_size_y
      - .offset:         104
        .size:           2
        .value_kind:     hidden_group_size_z
      - .offset:         106
        .size:           2
        .value_kind:     hidden_remainder_x
      - .offset:         108
        .size:           2
        .value_kind:     hidden_remainder_y
      - .offset:         110
        .size:           2
        .value_kind:     hidden_remainder_z
      - .offset:         128
        .size:           8
        .value_kind:     hidden_global_offset_x
      - .offset:         136
        .size:           8
        .value_kind:     hidden_global_offset_y
      - .offset:         144
        .size:           8
        .value_kind:     hidden_global_offset_z
      - .offset:         152
        .size:           2
        .value_kind:     hidden_grid_dims
      - .offset:         208
        .size:           4
        .value_kind:     hidden_dynamic_lds_size
    .group_segment_fixed_size: 0
    .kernarg_segment_align: 8
    .kernarg_segment_size: 344
    .language:       OpenCL C
    .language_version:
      - 2
      - 0
    .max_flat_workgroup_size: 512
    .name:           _Z12gemm_persistILi1ELi14336ELi32ELi16EEvPKDF16_S1_PvPKfS4_S4_S4_PDF16_S5_iii
    .private_segment_fixed_size: 0
    .sgpr_count:     72
    .sgpr_spill_count: 0
    .symbol:         _Z12gemm_persistILi1ELi14336ELi32ELi16EEvPKDF16_S1_PvPKfS4_S4_S4_PDF16_S5_iii.kd
    .uniform_work_group_size: 1
    .uses_dynamic_stack: false
    .vgpr_count:     236
    .vgpr_spill_count: 0
    .wavefront_size: 64
